# speedup vs baseline: 1.0080x; 1.0080x over previous
.Lk_304:
	s_andn2_saveexec_b64 s[56:57], s[56:57]
	s_cbranch_execz .Lk_287
	v_add_u32_e32 v178, 1, v177
	v_lshlrev_b32_e32 v12, 4, v178
	v_cmp_ne_u32_e64 s[10:11], 47, v177
	s_and_b64 vcc, exec, s[6:7]
	v_cndmask_b32_e64 v12, v174, v12, s[10:11]
	v_lshl_add_u32 v12, v12, 2, v169
	ds_read_b32 v179, v12
	s_cbranch_vccz .Lmy_gen

.Lmy_rd8:
	ds_read_b64 v[228:229], v208
	ds_read_b64 v[230:231], v209
	ds_read_b64 v[232:233], v210
	ds_read_b64 v[234:235], v211
	ds_read_b64 v[236:237], v212
	ds_read_b64 v[238:239], v213
	ds_read_b64 v[240:241], v214
	ds_read_b64 v[242:243], v215
	s_waitcnt lgkmcnt(7)
	v_fma_f32 v180, v228, v218, 0
	s_waitcnt lgkmcnt(6)
	v_fmac_f32_e32 v180, v230, v219
	s_waitcnt lgkmcnt(5)
	v_fmac_f32_e32 v180, v232, v220
	s_waitcnt lgkmcnt(4)
	v_fmac_f32_e32 v180, v234, v221
	s_waitcnt lgkmcnt(3)
	v_fmac_f32_e32 v180, v236, v222
	s_waitcnt lgkmcnt(2)
	v_fmac_f32_e32 v180, v238, v223
	s_waitcnt lgkmcnt(1)
	v_fmac_f32_e32 v180, v240, v224
	s_waitcnt lgkmcnt(0)
	v_fmac_f32_e32 v180, v242, v225
	s_cbranch_vccnz .Lk_318
	v_fmac_f32_e32 v180, v244, v226
	v_fmac_f32_e32 v180, v246, v227
	s_andn2_b64 vcc, exec, s[20:21]
	s_cbranch_vccnz .Lk_318
	v_lshlrev_b32_e32 v181, 12, v177
	v_and_b32_e32 v12, 0xf000, v181
	v_add_u16_e32 v46, v12, v120
	ds_read_b64 v[60:61], v46
	v_add_u16_e32 v46, v12, v119
	ds_read_b64 v[62:63], v46
	v_mul_f32_e32 v64, v112, v28
	s_andn2_b64 vcc, exec, s[22:23]
	s_waitcnt lgkmcnt(1)
	v_mul_f32_e32 v46, v115, v61
	v_cmp_class_f32_e64 s[58:59], v60, 64
	v_fma_f32 v28, v46, v54, v28
	v_fmac_f32_e32 v180, v60, v64
	v_cndmask_b32_e64 v46, -v117, v173, s[58:59]
	v_fmac_f32_e32 v28, v46, v55
	v_mul_f32_e32 v46, v113, v29
	s_waitcnt lgkmcnt(0)
	v_fmac_f32_e32 v180, v62, v46
	v_mul_f32_e32 v46, v116, v63
	v_cmp_class_f32_e64 s[58:59], v62, 64
	v_fma_f32 v29, v46, v54, v29
	v_med3_f32 v28, v28, v93, 0
	v_cndmask_b32_e64 v46, -v118, v173, s[58:59]
	v_fmac_f32_e32 v29, v46, v55
	v_med3_f32 v29, v29, v94, 0
	s_cbranch_vccnz .Lk_318
	v_add_u16_e32 v46, v12, v114
	v_add_u16_e32 v62, v12, v111
	v_add_u16_e32 v64, v12, v17
	v_add_u16_e32 v12, v12, v8
	ds_read_b64 v[60:61], v46
	ds_read_b64 v[62:63], v62
	ds_read_b64 v[64:65], v64
	ds_read_b64 v[72:73], v12
	v_mul_f32_e32 v12, v100, v30
	s_waitcnt lgkmcnt(3)
	v_fmac_f32_e32 v180, v60, v12
	v_mul_f32_e32 v12, v103, v61
	v_cmp_class_f32_e64 s[58:59], v60, 64
	v_fma_f32 v12, v12, v54, v30
	s_nop 0
	v_cndmask_b32_e64 v30, -v107, v173, s[58:59]
	v_fmac_f32_e32 v12, v30, v55
	v_med3_f32 v30, v12, v95, 0
	v_mul_f32_e32 v12, v101, v31
	s_waitcnt lgkmcnt(2)
	v_fmac_f32_e32 v180, v62, v12
	v_mul_f32_e32 v12, v104, v63
	v_cmp_class_f32_e64 s[58:59], v62, 64
	v_fma_f32 v12, v12, v54, v31
	s_nop 0
	v_cndmask_b32_e64 v31, -v108, v173, s[58:59]
	v_fmac_f32_e32 v12, v31, v55
	v_med3_f32 v31, v12, v96, 0
	v_mul_f32_e32 v12, v102, v32
	s_waitcnt lgkmcnt(1)
	v_fmac_f32_e32 v180, v64, v12
	v_mul_f32_e32 v12, v105, v65
	v_cmp_class_f32_e64 s[58:59], v64, 64
	v_fma_f32 v12, v12, v54, v32
	s_nop 0
	v_cndmask_b32_e64 v32, -v109, v173, s[58:59]
	v_fmac_f32_e32 v12, v32, v55
	v_med3_f32 v32, v12, v97, 0
	v_mul_f32_e32 v12, v16, v33
	s_waitcnt lgkmcnt(0)
	v_fmac_f32_e32 v180, v72, v12
	v_mul_f32_e32 v12, v106, v73
	v_cmp_class_f32_e64 s[58:59], v72, 64
	v_fmac_f32_e32 v33, v12, v54
	s_nop 0
	v_cndmask_b32_e64 v12, -v110, v173, s[58:59]
	v_fmac_f32_e32 v33, v12, v55
	v_med3_f32 v33, v33, v99, 0

.Lmy_gen:
	v_lshlrev_b32_e32 v181, 12, v177
	v_add_u32_e32 v12, 0xf000, v181
	v_add_u32_e32 v46, 0xe000, v181
	v_add_u32_e32 v60, 0xc000, v181
	v_and_or_b32 v182, v60, s3, v171
	v_and_or_b32 v183, v46, s3, v171
	v_and_or_b32 v184, v12, s3, v171
	v_mov_b32_e32 v180, 0
	s_mov_b32 s60, 0
	v_mov_b64_e32 v[60:61], v[42:43]
	v_mov_b64_e32 v[62:63], v[40:41]
	v_mov_b32_e32 v12, v172
	s_branch .Lk_308
